# P2 in-proj epilogue, silu-kind tiles: dropped the conservative vmcnt(0) in the last first-half row group (no loads pending on that path; prefetch and stores stay in flight)
# speedup vs baseline: 1.0052x; 1.0014x over previous
.LBB0_378:
	s_andn2_b64 vcc, exec, s[0:1]
	s_cbranch_vccnz .LBB0_380
	v_mul_f32_e32 v131, 0xbfb8aa3b, v10
	v_mul_f32_e32 v132, 0xbfb8aa3b, v15
	v_exp_f32_e32 v131, v131
	v_exp_f32_e32 v133, v132
	v_mul_f32_e32 v135, 0xbfb8aa3b, v12
	v_mul_f32_e32 v136, 0xbfb8aa3b, v17
	v_add_f32_e32 v131, 1.0, v131
	v_mul_f32_e32 v130, 0xbfb8aa3b, v14
	v_rcp_f32_e32 v132, v131
	v_add_f32_e32 v131, 1.0, v133
	v_mul_f32_e32 v133, 0xbfb8aa3b, v11
	v_mul_f32_e32 v134, 0xbfb8aa3b, v16
	v_exp_f32_e32 v135, v135
	v_exp_f32_e32 v137, v136
	v_mul_f32_e32 v136, 0xbfb8aa3b, v13
	v_exp_f32_e32 v130, v130
	v_exp_f32_e32 v133, v133
	v_exp_f32_e32 v134, v134
	v_exp_f32_e32 v146, v136
	v_add_f32_e32 v135, 1.0, v135
	v_add_f32_e32 v130, 1.0, v130
	v_add_f32_e32 v133, 1.0, v133
	v_add_f32_e32 v134, 1.0, v134
	v_rcp_f32_e32 v136, v135
	v_add_f32_e32 v135, 1.0, v137
	v_add_f32_e32 v137, 1.0, v146
	v_rcp_f32_e32 v130, v130
	v_rcp_f32_e32 v131, v131
	v_rcp_f32_e32 v134, v134
	v_rcp_f32_e32 v135, v135
	v_rcp_f32_e32 v137, v137
	v_rcp_f32_e32 v133, v133
	v_pk_mul_f32 v[186:187], v[14:15], v[130:131]
	v_pk_mul_f32 v[190:191], v[16:17], v[134:135]
	v_pk_mul_f32 v[192:193], v[12:13], v[136:137]
	v_pk_mul_f32 v[188:189], v[10:11], v[132:133]
